# speedup vs baseline: 1.0236x; 1.0236x over previous
.LBB2_8:
	s_or_b64 exec, exec, s[2:3]
	s_lshl_b32 s39, s38, 11
	s_add_i32 s39, s39, 0x22000
	s_mul_hi_i32 s2, s10, 0x980
	s_mulk_i32 s10, 0x980
	s_movk_i32 s4, 0x980
	s_waitcnt lgkmcnt(0)
	s_add_u32 s36, s30, s10
	v_mov_b64_e32 v[8:9], s[30:31]
	s_addc_u32 s37, s31, s2
	v_mad_u64_u32 v[8:9], s[2:3], v2, s4, v[8:9]
	v_mov_b32_e32 v2, v9
	v_mad_u64_u32 v[2:3], s[2:3], v3, s4, v[2:3]
	v_mov_b32_e32 v5, 0
	v_and_b32_e32 v4, 60, v110
	v_mov_b32_e32 v9, v2
	v_lshl_add_u64 v[2:3], v[8:9], 0, v[4:5]
	global_load_dword v6, v4, s[36:37]
	global_load_dword v11, v[2:3], off
	v_and_b32_e32 v114, 3, v0
	v_cmp_eq_u32_e64 s[2:3], 0, v114
	s_mov_b32 s4, 0
	v_lshrrev_b32_e32 v34, 2, v110
	s_mov_b32 s6, s4
	s_mov_b32 s7, s4
	v_mul_u32_u24_e32 v7, 0x30d4, v34
	s_mov_b32 s5, s4
	v_mov_b32_e32 v117, v5
	v_mov_b64_e32 v[16:17], s[6:7]
	v_lshlrev_b32_e32 v116, 2, v7
	v_mov_b32_e32 v12, v5
	v_lshl_or_b32 v8, v110, 4, s39
	v_mov_b64_e32 v[14:15], s[4:5]
	v_lshl_add_u64 v[118:119], s[34:35], 0, v[116:117]
	v_lshlrev_b32_e32 v36, 2, v114
	ds_write_b128 v8, v[14:17]
	ds_write_b128 v8, v[14:17] offset:1024
	s_mul_i32 s84, s38, 0x2400
	v_lshl_add_u32 v200, v110, 4, s84
	ds_write_b128 v200, v[14:17]
	ds_write_b128 v200, v[14:17] offset:1024
	ds_write_b128 v200, v[14:17] offset:2048
	ds_write_b128 v200, v[14:17] offset:3072
	ds_write_b128 v200, v[14:17] offset:4096
	ds_write_b128 v200, v[14:17] offset:5120
	ds_write_b128 v200, v[14:17] offset:6144
	ds_write_b128 v200, v[14:17] offset:7168
	ds_write_b128 v200, v[14:17] offset:8192
	v_mov_b32_e32 v15, v5
	s_waitcnt vmcnt(1)
	v_ashrrev_i32_e32 v7, 31, v6
	s_waitcnt vmcnt(0)
	v_sub_u32_e32 v10, v11, v6
	v_cndmask_b32_e64 v13, 0, v10, s[2:3]
	v_lshl_add_u64 v[8:9], v[6:7], 2, v[118:119]
	v_cmp_lt_i32_e32 vcc, v114, v10
	v_add_u32_dpp v13, v13, v13 row_shr:1 row_mask:0xf bank_mask:0xf bound_ctrl:1
	s_nop 1
	v_add_u32_dpp v13, v13, v13 row_shr:2 row_mask:0xf bank_mask:0xf bound_ctrl:1
	s_nop 1
	v_add_u32_dpp v13, v13, v13 row_shr:4 row_mask:0xf bank_mask:0xf bound_ctrl:1
	s_nop 1
	v_add_u32_dpp v13, v13, v13 row_shr:8 row_mask:0xf bank_mask:0xf bound_ctrl:1
	s_nop 1
	v_add_u32_dpp v13, v13, v13 row_bcast:15 row_mask:0xa bank_mask:0xf
	s_nop 1
	v_mov_b32_dpp v12, v13 row_bcast:31 row_mask:0xc bank_mask:0xf
	s_and_saveexec_b64 s[4:5], vcc
	s_cbranch_execz .LBB2_10
	v_mov_b32_e32 v37, 0
	v_lshl_add_u64 v[14:15], v[8:9], 0, v[36:37]
	global_load_dword v15, v[14:15], off

.LBB2_62:
	s_cmp_eq_u32 s49, 0
	s_cselect_b64 s[6:7], -1, 0
	s_cmp_lg_u32 s49, 0
	s_cbranch_scc0 .LBB2_93
	v_cndmask_b32_e64 v34, 0, 1, s[6:7]
	v_cmp_ne_u32_e64 s[0:1], 1, v34
.LBB2_64:
	s_mov_b64 s[54:55], s[6:7]
	s_lshl_b32 s66, s49, 6
	s_sub_i32 s66, s41, s66
	s_cmp_gt_i32 s66, 32
	s_cselect_b64 s[80:81], -1, 0
	v_bfe_u32 v34, v121, 16, 4
	v_cmp_gt_i32_e64 s[56:57], s66, v110
	v_lshl_add_u32 v115, v34, 1, v191
	v_lshlrev_b32_e32 v34, 2, v34
	ds_bpermute_b32 v121, v34, v197
	v_xor_b32_e32 v34, 64, v122
	ds_read_b128 v[208:211], v122
	ds_read_b128 v[212:215], v34
	ds_read_b128 v[216:219], v122 offset:2048
	ds_read_b128 v[220:223], v34 offset:2048
	ds_read_b128 v[224:227], v122 offset:4096
	ds_read_b128 v[228:231], v34 offset:4096
	ds_read_b128 v[232:235], v122 offset:6144
	ds_read_b128 v[236:239], v34 offset:6144
	ds_read_b64_tr_b16 v[130:131], v186 offset:0
	ds_read_b64_tr_b16 v[132:133], v186 offset:2048
	ds_read_b64_tr_b16 v[134:135], v188 offset:0
	ds_read_b64_tr_b16 v[136:137], v188 offset:2048
	ds_read_b64_tr_b16 v[138:139], v189 offset:0
	ds_read_b64_tr_b16 v[140:141], v189 offset:2048
	ds_read_b64_tr_b16 v[142:143], v190 offset:0
	ds_read_b64_tr_b16 v[144:145], v190 offset:2048
	s_and_b64 vcc, exec, s[54:55]
	s_cbranch_vccz .Lmk_ua_ready
	s_waitcnt vmcnt(8)
.Lmk_ua_ready:
	s_waitcnt lgkmcnt(8)
	v_mfma_f32_16x16x32_f16 v[200:203], v[240:243], v[208:211], 0
	v_mfma_f32_16x16x32_f16 v[160:163], v[240:243], v[216:219], 0
	v_mfma_f32_16x16x32_f16 v[248:251], v[240:243], v[224:227], 0
	v_mfma_f32_16x16x32_f16 v[252:255], v[240:243], v[232:235], 0
	v_mfma_f32_16x16x32_f16 v[200:203], v[244:247], v[212:215], v[200:203]
	v_mfma_f32_16x16x32_f16 v[160:163], v[244:247], v[220:223], v[160:163]
	v_mfma_f32_16x16x32_f16 v[248:251], v[244:247], v[228:231], v[248:251]
	v_mfma_f32_16x16x32_f16 v[252:255], v[244:247], v[236:239], v[252:255]
	ds_read_b64_tr_b16 v[146:147], v186 offset:4096
	ds_read_b64_tr_b16 v[148:149], v186 offset:6144
	ds_read_b64_tr_b16 v[150:151], v188 offset:4096
	ds_read_b64_tr_b16 v[152:153], v188 offset:6144
	ds_read_b64_tr_b16 v[154:155], v189 offset:4096
	ds_read_b64_tr_b16 v[156:157], v189 offset:6144
	ds_read_b64_tr_b16 v[204:205], v190 offset:4096
	ds_read_b64_tr_b16 v[206:207], v190 offset:6144
	v_cndmask_b32_e64 v34, v200, v160, s[60:61]
	v_cndmask_b32_e64 v34, v34, v248, s[62:63]
	v_cndmask_b32_e64 v34, v34, v252, s[64:65]
	v_cndmask_b32_e64 v201, v195, v185, s[54:55]
	v_add_f32_e32 v202, 0x40200000, v201
	v_add_f32_e32 v34, v34, v121
	v_mul_f32_e32 v121, 0x3e4ccccd, v34
	v_max_f32_e32 v34, v34, v121
	v_cmp_gt_f32_e32 vcc, v34, v202
	s_and_b64 s[68:69], s[56:57], vcc
	s_cmp_eq_u64 s[68:69], 0
	s_cbranch_scc1 .Lmk_nomax_pre
	v_cndmask_b32_e64 v161, v185, v34, s[56:57]
	s_lshl_b32 s6, s43, 6
	s_sub_i32 s83, s44, s6
	v_max_f32_dpp v161, v161, v161 row_shr:1 row_mask:0xf bank_mask:0xf
	s_lshl_b32 s6, s43, 8
	s_add_i32 s82, s78, s6
	v_max_f32_dpp v161, v161, v161 row_shr:2 row_mask:0xf bank_mask:0xf
	v_add_u32_e32 v229, s82, v172
	v_add_u32_e32 v230, s82, v173
	v_max_f32_dpp v161, v161, v161 row_shr:4 row_mask:0xf bank_mask:0xf
	ds_read_b32 v224, v229 offset:0
	ds_read_b32 v225, v229 offset:32
	v_max_f32_dpp v161, v161, v161 row_shr:8 row_mask:0xf bank_mask:0xf
	ds_read_b32 v226, v229 offset:64
	ds_read_b32 v227, v229 offset:96
	v_max_f32_dpp v161, v161, v161 row_bcast:15 row_mask:0xa bank_mask:0xf
	ds_read_b32 v232, v229 offset:128
	ds_read_b32 v233, v229 offset:160
	v_max_f32_dpp v161, v161, v161 row_bcast:31 row_mask:0xc bank_mask:0xf
	ds_read_b32 v234, v229 offset:192
	ds_read_b32 v235, v229 offset:224
	v_readlane_b32 s70, v161, 63
	ds_read_b32 v198, v230
	v_mov_b64_e32 v[208:209], s[12:13]
	v_mov_b64_e32 v[210:211], s[12:13]
	s_and_b64 vcc, exec, s[54:55]
	s_nop 0
	v_mov_b32_e32 v161, s70
	s_cbranch_vccnz .Lmk_norescale
	v_sub_f32_e32 v162, v195, v161
	v_mul_f32_e32 v162, 0x3fb8aa3b, v162
	v_exp_f32_e32 v248, v162
	s_nop 0
	v_pk_mul_f32 v[56:57], v[248:249], v[56:57] op_sel_hi:[0,1]
	v_pk_mul_f32 v[54:55], v[248:249], v[54:55] op_sel_hi:[0,1]
	v_pk_mul_f32 v[60:61], v[248:249], v[60:61] op_sel_hi:[0,1]
	v_pk_mul_f32 v[58:59], v[248:249], v[58:59] op_sel_hi:[0,1]
	v_pk_mul_f32 v[64:65], v[248:249], v[64:65] op_sel_hi:[0,1]
	v_pk_mul_f32 v[62:63], v[248:249], v[62:63] op_sel_hi:[0,1]
	v_pk_mul_f32 v[68:69], v[248:249], v[68:69] op_sel_hi:[0,1]
	v_pk_mul_f32 v[66:67], v[248:249], v[66:67] op_sel_hi:[0,1]
	v_pk_mul_f32 v[72:73], v[72:73], v[248:249] op_sel_hi:[1,0]
	v_pk_mul_f32 v[70:71], v[70:71], v[248:249] op_sel_hi:[1,0]
.Lmk_norescale:
	v_mov_b32_e32 v201, v161
	s_branch .Lmk_nomax
.Lmk_nomax_pre:
	s_lshl_b32 s6, s43, 6
	s_sub_i32 s83, s44, s6
	s_lshl_b32 s6, s43, 8
	s_add_i32 s82, s78, s6
	v_add_u32_e32 v229, s82, v172
	v_add_u32_e32 v230, s82, v173
	ds_read_b32 v224, v229 offset:0
	ds_read_b32 v225, v229 offset:32
	ds_read_b32 v226, v229 offset:64
	ds_read_b32 v227, v229 offset:96
	ds_read_b32 v232, v229 offset:128
	ds_read_b32 v233, v229 offset:160
	ds_read_b32 v234, v229 offset:192
	ds_read_b32 v235, v229 offset:224
	ds_read_b32 v198, v230
	v_mov_b64_e32 v[208:209], s[12:13]
	v_mov_b64_e32 v[210:211], s[12:13]

.Lmk_wdone:
	s_waitcnt lgkmcnt(0)
	s_and_b64 vcc, exec, s[54:55]
	s_cbranch_vccnz .Lmk_agg_first
	v_mfma_f32_16x16x32_f16 v[54:57], v[130:133], v[200:203], v[54:57]
	ds_write_b16 v115, v35
	ds_write_b128 v196, v[10:13]
	v_mfma_f32_16x16x32_f16 v[58:61], v[134:137], v[200:203], v[58:61]
	ds_write_b128 v196, v[14:17] offset:1024
	v_mfma_f32_16x16x32_f16 v[62:65], v[138:141], v[200:203], v[62:65]
	ds_write_b128 v196, v[30:33] offset:2048
	v_mfma_f32_16x16x32_f16 v[66:69], v[142:145], v[200:203], v[66:69]
	ds_write_b128 v196, v[26:29] offset:3072
	v_mfma_f32_16x16x32_f16 v[70:73], v[208:211], v[200:203], v[70:73]
	s_branch .Lmk_agg_join
.Lmk_agg_first:
	v_mfma_f32_16x16x32_f16 v[54:57], v[130:133], v[200:203], 0
	ds_write_b16 v115, v35
	ds_write_b128 v196, v[10:13]
	v_mfma_f32_16x16x32_f16 v[58:61], v[134:137], v[200:203], 0
	ds_write_b128 v196, v[14:17] offset:1024
	v_mfma_f32_16x16x32_f16 v[62:65], v[138:141], v[200:203], 0
	ds_write_b128 v196, v[30:33] offset:2048
	v_mfma_f32_16x16x32_f16 v[66:69], v[142:145], v[200:203], 0
	ds_write_b128 v196, v[26:29] offset:3072
	v_mfma_f32_16x16x32_f16 v[70:73], v[208:211], v[200:203], 0
.Lmk_agg_join:
	s_andn2_b64 vcc, exec, s[30:31]
	s_cbranch_vccnz .Lmk_st_done
	ds_write_b128 v196, v[2:5] offset:4096
	ds_write_b128 v196, v[6:9] offset:5120
	ds_write_b128 v196, v[18:21] offset:6144
	ds_write_b128 v196, v[22:25] offset:7168

.Lmk_gather:
	v_and_b32_e32 v10, 0xffff, v224
	v_and_b32_e32 v14, 0xffff, v225
	v_and_b32_e32 v30, 0xffff, v226
	v_and_b32_e32 v26, 0xffff, v227
	s_cmp_gt_i32 s83, 32
	v_lshl_or_b32 v10, v10, 7, v176
	v_lshl_or_b32 v14, v14, 7, v176
	s_cselect_b64 s[30:31], -1, 0
	v_lshl_or_b32 v30, v30, 7, v176
	v_lshl_or_b32 v26, v26, 7, v176
	s_cmp_lt_i32 s83, 33
	global_load_dwordx4 v[10:13], v10, s[28:29]
	global_load_dwordx4 v[14:17], v14, s[28:29]
	global_load_dwordx4 v[30:33], v30, s[28:29]
	global_load_dwordx4 v[26:29], v26, s[28:29]
	s_cbranch_scc1 .LBB2_68
	v_and_b32_e32 v2, 0xffff, v232
	v_and_b32_e32 v6, 0xffff, v233
	v_and_b32_e32 v18, 0xffff, v234
	v_and_b32_e32 v22, 0xffff, v235
	v_lshl_or_b32 v2, v2, 7, v176
	v_lshl_or_b32 v6, v6, 7, v176
	v_lshl_or_b32 v18, v18, 7, v176
	v_lshl_or_b32 v22, v22, 7, v176
	global_load_dwordx4 v[2:5], v2, s[28:29]
	global_load_dwordx4 v[6:9], v6, s[28:29]
	global_load_dwordx4 v[18:21], v18, s[28:29]
	global_load_dwordx4 v[22:25], v22, s[28:29]

.LBB2_107:
	v_cndmask_b32_e64 v34, 0, 1, s[6:7]
	v_cmp_ne_u32_e64 s[0:1], 1, v34
	s_branch .LBB2_64
